# scoring loop: 4 fewer VALU per key tile (bitop3 score code, no masking of never-read codes) and static s_setprio 1 for waves 4-7 inside the loop
# speedup vs baseline: 1.0167x; 1.0028x over previous
.Lq_pre:
	v_readlane_b32 s42, v254, 40
	v_readlane_b32 s43, v254, 41
	s_mov_b32 s63, 0x20000
	s_mov_b32 s64, 0x8000
	v_readlane_b32 s65, v253, 0
	s_cmp_lt_u32 s65, 4
	s_cbranch_scc1 .Lq_noprio
	s_setprio 1
.Lq_noprio:
	v_lshlrev_b32_e32 v238, 4, v114
	v_mov_b32_e32 v239, 0xc00
	v_add_u32_e32 v237, 0xffff0000, v202
	s_add_u32 s42, s42, 0x24000000
	s_addc_u32 s43, s43, 0
	s_lshl_b32 s6, s6, 12
	s_add_u32 s12, s42, s6
	s_addc_u32 s13, s43, 0
	global_load_dwordx4 v[110:113], v238, s[12:13]
	global_load_dwordx4 v[106:109], v238, s[12:13] offset:1024
	global_load_dwordx4 v[102:105], v238, s[12:13] offset:2048
	global_load_dwordx4 v[98:101], v238, s[12:13] offset:3072
	s_waitcnt vmcnt(4)
	v_mfma_f32_32x32x16_bf16 v[206:221], v[42:45], v[94:97], 0
	v_mfma_f32_32x32x16_bf16 v[206:221], v[34:37], v[86:89], v[206:221]
	v_mfma_f32_32x32x16_bf16 v[206:221], v[38:41], v[82:85], v[206:221]
	v_mfma_f32_32x32x16_bf16 v[206:221], v[46:49], v[74:77], v[206:221]
	s_nop 11
.Lq_loop:
	s_cmp_ge_u32 s11, s9
	s_cbranch_scc1 .Lq_end
	v_add_u32_e32 v204, 0xfffffe00, v203
	v_cmp_le_i32_e64 s[44:45], v204, v185
	v_cmp_le_i32_e64 s[46:47], v204, v201
	v_mfma_f32_32x32x16_bf16 v[0:15], v[58:61], v[94:97], 0
	v_fma_f32 v16, v127, v206, 0
	v_fma_f32 v17, v161, v214, 0
	v_fma_f32 v16, v127, |v206|, v16
	v_fma_f32 v17, v161, |v214|, v17
	v_fmac_f32_e32 v16, v155, v207
	v_fmac_f32_e32 v17, v163, v215
	v_fma_f32 v16, v155, |v207|, v16
	v_fma_f32 v17, v163, |v215|, v17
	v_fmac_f32_e32 v16, v157, v208
	v_fmac_f32_e32 v17, v165, v216
	v_mfma_f32_32x32x16_bf16 v[0:15], v[50:53], v[86:89], v[0:15]
	v_fma_f32 v16, v157, |v208|, v16
	v_fma_f32 v17, v165, |v216|, v17
	v_fmac_f32_e32 v16, v159, v209
	v_fmac_f32_e32 v17, v167, v217
	v_fma_f32 v16, v159, |v209|, v16
	v_fma_f32 v17, v167, |v217|, v17
	v_fmac_f32_e32 v16, v136, v210
	v_fmac_f32_e32 v17, v162, v218
	v_fma_f32 v16, v136, |v210|, v16
	v_fma_f32 v17, v162, |v218|, v17
	v_mfma_f32_32x32x16_bf16 v[0:15], v[54:57], v[82:85], v[0:15]
	v_fmac_f32_e32 v16, v156, v211
	v_fmac_f32_e32 v17, v164, v219
	v_fma_f32 v16, v156, |v211|, v16
	v_fma_f32 v17, v164, |v219|, v17
	v_fmac_f32_e32 v16, v158, v212
	v_fmac_f32_e32 v17, v166, v220
	v_fma_f32 v16, v158, |v212|, v16
	v_fma_f32 v17, v166, |v220|, v17
	v_fmac_f32_e32 v16, v160, v213
	v_fmac_f32_e32 v17, v168, v221
	v_mfma_f32_32x32x16_bf16 v[0:15], v[62:65], v[74:77], v[0:15]
	v_fma_f32 v16, v160, |v213|, v16
	v_fma_f32 v17, v168, |v221|, v17
	s_nop 1
	v_permlane32_swap_b32_e32 v16, v17
	v_add_f32_e32 v18, v16, v17
	v_cvt_f16_f32_e32 v18, v18
	v_ashrrev_i16_e32 v19, 15, v18
	v_bitop3_b32 v20, v18, v19, s64 bitop3:0x1e
	v_or_b32_sdwa v21, v147, v20 dst_sel:DWORD dst_unused:UNUSED_PAD src0_sel:DWORD src1_sel:BYTE_1
	v_cndmask_b32_e64 v21, v239, v21, s[44:45]
	ds_write_b16 v237, v20
	v_lshl_add_u32 v21, v21, 2, s63
	ds_add_u32 v21, v187
	s_add_i32 s6, s10, -16
	s_min_i32 s6, s6, s8
	s_lshl_b32 s6, s6, 12
	s_add_u32 s12, s42, s6
	s_addc_u32 s13, s43, 0
	global_load_dwordx4 v[94:97], v238, s[12:13]
	global_load_dwordx4 v[86:89], v238, s[12:13] offset:1024
	global_load_dwordx4 v[82:85], v238, s[12:13] offset:2048
	global_load_dwordx4 v[74:77], v238, s[12:13] offset:3072
	s_waitcnt vmcnt(8)
	v_mfma_f32_32x32x16_bf16 v[206:221], v[42:45], v[90:93], 0
	v_fma_f32 v22, v169, v0, 0
	v_fma_f32 v23, v177, v8, 0
	v_fma_f32 v22, v169, |v0|, v22
	v_fma_f32 v23, v177, |v8|, v23
	v_fmac_f32_e32 v22, v171, v1
	v_fmac_f32_e32 v23, v179, v9
	v_fma_f32 v22, v171, |v1|, v22
	v_fma_f32 v23, v179, |v9|, v23
	v_fmac_f32_e32 v22, v173, v2
	v_fmac_f32_e32 v23, v181, v10
	v_mfma_f32_32x32x16_bf16 v[206:221], v[34:37], v[78:81], v[206:221]
	v_fma_f32 v22, v173, |v2|, v22
	v_fma_f32 v23, v181, |v10|, v23
	v_fmac_f32_e32 v22, v175, v3
	v_fmac_f32_e32 v23, v183, v11
	v_fma_f32 v22, v175, |v3|, v22
	v_fma_f32 v23, v183, |v11|, v23
	v_fmac_f32_e32 v22, v170, v4
	v_fmac_f32_e32 v23, v178, v12
	v_fma_f32 v22, v170, |v4|, v22
	v_fma_f32 v23, v178, |v12|, v23
	v_mfma_f32_32x32x16_bf16 v[206:221], v[38:41], v[70:73], v[206:221]
	v_fmac_f32_e32 v22, v172, v5
	v_fmac_f32_e32 v23, v180, v13
	v_fma_f32 v22, v172, |v5|, v22
	v_fma_f32 v23, v180, |v13|, v23
	v_fmac_f32_e32 v22, v174, v6
	v_fmac_f32_e32 v23, v182, v14
	v_fma_f32 v22, v174, |v6|, v22
	v_fma_f32 v23, v182, |v14|, v23
	v_fmac_f32_e32 v22, v176, v7
	v_fmac_f32_e32 v23, v184, v15
	v_mfma_f32_32x32x16_bf16 v[206:221], v[46:49], v[66:69], v[206:221]
	v_fma_f32 v22, v176, |v7|, v22
	v_fma_f32 v23, v184, |v15|, v23
	s_nop 1
	v_permlane32_swap_b32_e32 v22, v23
	v_add_f32_e32 v24, v22, v23
	v_cvt_f16_f32_e32 v24, v24
	v_ashrrev_i16_e32 v25, 15, v24
	v_bitop3_b32 v26, v24, v25, s64 bitop3:0x1e
	v_or_b32_sdwa v27, v149, v26 dst_sel:DWORD dst_unused:UNUSED_PAD src0_sel:DWORD src1_sel:BYTE_1
	v_cndmask_b32_e64 v27, v239, v27, s[46:47]
	ds_write_b16 v202, v26
	v_lshl_add_u32 v27, v27, 2, s63
	ds_add_u32 v27, v187
	s_add_i32 s11, s11, 1
	s_cmp_ge_u32 s11, s9
	s_cbranch_scc1 .Lq_end
	v_add_u32_e32 v204, 0xffffff00, v203
	v_cmp_le_i32_e64 s[44:45], v204, v185
	v_cmp_le_i32_e64 s[46:47], v204, v201
	v_mfma_f32_32x32x16_bf16 v[0:15], v[58:61], v[90:93], 0
	v_fma_f32 v16, v127, v206, 0
	v_fma_f32 v17, v161, v214, 0
	v_fma_f32 v16, v127, |v206|, v16
	v_fma_f32 v17, v161, |v214|, v17
	v_fmac_f32_e32 v16, v155, v207
	v_fmac_f32_e32 v17, v163, v215
	v_fma_f32 v16, v155, |v207|, v16
	v_fma_f32 v17, v163, |v215|, v17
	v_fmac_f32_e32 v16, v157, v208
	v_fmac_f32_e32 v17, v165, v216
	v_mfma_f32_32x32x16_bf16 v[0:15], v[50:53], v[78:81], v[0:15]
	v_fma_f32 v16, v157, |v208|, v16
	v_fma_f32 v17, v165, |v216|, v17
	v_fmac_f32_e32 v16, v159, v209
	v_fmac_f32_e32 v17, v167, v217
	v_fma_f32 v16, v159, |v209|, v16
	v_fma_f32 v17, v167, |v217|, v17
	v_fmac_f32_e32 v16, v136, v210
	v_fmac_f32_e32 v17, v162, v218
	v_fma_f32 v16, v136, |v210|, v16
	v_fma_f32 v17, v162, |v218|, v17
	v_mfma_f32_32x32x16_bf16 v[0:15], v[54:57], v[70:73], v[0:15]
	v_fmac_f32_e32 v16, v156, v211
	v_fmac_f32_e32 v17, v164, v219
	v_fma_f32 v16, v156, |v211|, v16
	v_fma_f32 v17, v164, |v219|, v17
	v_fmac_f32_e32 v16, v158, v212
	v_fmac_f32_e32 v17, v166, v220
	v_fma_f32 v16, v158, |v212|, v16
	v_fma_f32 v17, v166, |v220|, v17
	v_fmac_f32_e32 v16, v160, v213
	v_fmac_f32_e32 v17, v168, v221
	v_mfma_f32_32x32x16_bf16 v[0:15], v[62:65], v[66:69], v[0:15]
	v_fma_f32 v16, v160, |v213|, v16
	v_fma_f32 v17, v168, |v221|, v17
	s_nop 1
	v_permlane32_swap_b32_e32 v16, v17
	v_add_f32_e32 v18, v16, v17
	v_cvt_f16_f32_e32 v18, v18
	v_ashrrev_i16_e32 v19, 15, v18
	v_bitop3_b32 v20, v18, v19, s64 bitop3:0x1e
	v_or_b32_sdwa v21, v147, v20 dst_sel:DWORD dst_unused:UNUSED_PAD src0_sel:DWORD src1_sel:BYTE_1
	v_cndmask_b32_e64 v21, v239, v21, s[44:45]
	ds_write_b16 v237, v20 offset:512
	v_lshl_add_u32 v21, v21, 2, s63
	ds_add_u32 v21, v187
	s_add_i32 s6, s10, -8
	s_min_i32 s6, s6, s8
	s_lshl_b32 s6, s6, 12
	s_add_u32 s12, s42, s6
	s_addc_u32 s13, s43, 0
	global_load_dwordx4 v[90:93], v238, s[12:13]
	global_load_dwordx4 v[78:81], v238, s[12:13] offset:1024
	global_load_dwordx4 v[70:73], v238, s[12:13] offset:2048
	global_load_dwordx4 v[66:69], v238, s[12:13] offset:3072
	s_waitcnt vmcnt(8)
	v_mfma_f32_32x32x16_bf16 v[206:221], v[42:45], v[110:113], 0
	v_fma_f32 v22, v169, v0, 0
	v_fma_f32 v23, v177, v8, 0
	v_fma_f32 v22, v169, |v0|, v22
	v_fma_f32 v23, v177, |v8|, v23
	v_fmac_f32_e32 v22, v171, v1
	v_fmac_f32_e32 v23, v179, v9
	v_fma_f32 v22, v171, |v1|, v22
	v_fma_f32 v23, v179, |v9|, v23
	v_fmac_f32_e32 v22, v173, v2
	v_fmac_f32_e32 v23, v181, v10
	v_mfma_f32_32x32x16_bf16 v[206:221], v[34:37], v[106:109], v[206:221]
	v_fma_f32 v22, v173, |v2|, v22
	v_fma_f32 v23, v181, |v10|, v23
	v_fmac_f32_e32 v22, v175, v3
	v_fmac_f32_e32 v23, v183, v11
	v_fma_f32 v22, v175, |v3|, v22
	v_fma_f32 v23, v183, |v11|, v23
	v_fmac_f32_e32 v22, v170, v4
	v_fmac_f32_e32 v23, v178, v12
	v_fma_f32 v22, v170, |v4|, v22
	v_fma_f32 v23, v178, |v12|, v23
	v_mfma_f32_32x32x16_bf16 v[206:221], v[38:41], v[102:105], v[206:221]
	v_fmac_f32_e32 v22, v172, v5
	v_fmac_f32_e32 v23, v180, v13
	v_fma_f32 v22, v172, |v5|, v22
	v_fma_f32 v23, v180, |v13|, v23
	v_fmac_f32_e32 v22, v174, v6
	v_fmac_f32_e32 v23, v182, v14
	v_fma_f32 v22, v174, |v6|, v22
	v_fma_f32 v23, v182, |v14|, v23
	v_fmac_f32_e32 v22, v176, v7
	v_fmac_f32_e32 v23, v184, v15
	v_mfma_f32_32x32x16_bf16 v[206:221], v[46:49], v[98:101], v[206:221]
	v_fma_f32 v22, v176, |v7|, v22
	v_fma_f32 v23, v184, |v15|, v23
	s_nop 1
	v_permlane32_swap_b32_e32 v22, v23
	v_add_f32_e32 v24, v22, v23
	v_cvt_f16_f32_e32 v24, v24
	v_ashrrev_i16_e32 v25, 15, v24
	v_bitop3_b32 v26, v24, v25, s64 bitop3:0x1e
	v_or_b32_sdwa v27, v149, v26 dst_sel:DWORD dst_unused:UNUSED_PAD src0_sel:DWORD src1_sel:BYTE_1
	v_cndmask_b32_e64 v27, v239, v27, s[46:47]
	ds_write_b16 v202, v26 offset:512
	v_lshl_add_u32 v27, v27, 2, s63
	ds_add_u32 v27, v187
	s_add_i32 s11, s11, 1
	s_cmp_ge_u32 s11, s9
	s_cbranch_scc1 .Lq_end
	v_mov_b32_e32 v204, v203
	v_cmp_le_i32_e64 s[44:45], v204, v185
	v_cmp_le_i32_e64 s[46:47], v204, v201
	v_mfma_f32_32x32x16_bf16 v[0:15], v[58:61], v[110:113], 0
	v_fma_f32 v16, v127, v206, 0
	v_fma_f32 v17, v161, v214, 0
	v_fma_f32 v16, v127, |v206|, v16
	v_fma_f32 v17, v161, |v214|, v17
	v_fmac_f32_e32 v16, v155, v207
	v_fmac_f32_e32 v17, v163, v215
	v_fma_f32 v16, v155, |v207|, v16
	v_fma_f32 v17, v163, |v215|, v17
	v_fmac_f32_e32 v16, v157, v208
	v_fmac_f32_e32 v17, v165, v216
	v_mfma_f32_32x32x16_bf16 v[0:15], v[50:53], v[106:109], v[0:15]
	v_fma_f32 v16, v157, |v208|, v16
	v_fma_f32 v17, v165, |v216|, v17
	v_fmac_f32_e32 v16, v159, v209
	v_fmac_f32_e32 v17, v167, v217
	v_fma_f32 v16, v159, |v209|, v16
	v_fma_f32 v17, v167, |v217|, v17
	v_fmac_f32_e32 v16, v136, v210
	v_fmac_f32_e32 v17, v162, v218
	v_fma_f32 v16, v136, |v210|, v16
	v_fma_f32 v17, v162, |v218|, v17
	v_mfma_f32_32x32x16_bf16 v[0:15], v[54:57], v[102:105], v[0:15]
	v_fmac_f32_e32 v16, v156, v211
	v_fmac_f32_e32 v17, v164, v219
	v_fma_f32 v16, v156, |v211|, v16
	v_fma_f32 v17, v164, |v219|, v17
	v_fmac_f32_e32 v16, v158, v212
	v_fmac_f32_e32 v17, v166, v220
	v_fma_f32 v16, v158, |v212|, v16
	v_fma_f32 v17, v166, |v220|, v17
	v_fmac_f32_e32 v16, v160, v213
	v_fmac_f32_e32 v17, v168, v221
	v_mfma_f32_32x32x16_bf16 v[0:15], v[62:65], v[98:101], v[0:15]
	v_fma_f32 v16, v160, |v213|, v16
	v_fma_f32 v17, v168, |v221|, v17
	s_nop 1
	v_permlane32_swap_b32_e32 v16, v17
	v_add_f32_e32 v18, v16, v17
	v_cvt_f16_f32_e32 v18, v18
	v_ashrrev_i16_e32 v19, 15, v18
	v_bitop3_b32 v20, v18, v19, s64 bitop3:0x1e
	v_or_b32_sdwa v21, v147, v20 dst_sel:DWORD dst_unused:UNUSED_PAD src0_sel:DWORD src1_sel:BYTE_1
	v_cndmask_b32_e64 v21, v239, v21, s[44:45]
	ds_write_b16 v237, v20 offset:1024
	v_lshl_add_u32 v21, v21, 2, s63
	ds_add_u32 v21, v187
	s_min_i32 s6, s10, s8
	s_lshl_b32 s6, s6, 12
	s_add_u32 s12, s42, s6
	s_addc_u32 s13, s43, 0
	global_load_dwordx4 v[110:113], v238, s[12:13]
	global_load_dwordx4 v[106:109], v238, s[12:13] offset:1024
	global_load_dwordx4 v[102:105], v238, s[12:13] offset:2048
	global_load_dwordx4 v[98:101], v238, s[12:13] offset:3072
	s_waitcnt vmcnt(8)
	v_mfma_f32_32x32x16_bf16 v[206:221], v[42:45], v[94:97], 0
	v_fma_f32 v22, v169, v0, 0
	v_fma_f32 v23, v177, v8, 0
	v_fma_f32 v22, v169, |v0|, v22
	v_fma_f32 v23, v177, |v8|, v23
	v_fmac_f32_e32 v22, v171, v1
	v_fmac_f32_e32 v23, v179, v9
	v_fma_f32 v22, v171, |v1|, v22
	v_fma_f32 v23, v179, |v9|, v23
	v_fmac_f32_e32 v22, v173, v2
	v_fmac_f32_e32 v23, v181, v10
	v_mfma_f32_32x32x16_bf16 v[206:221], v[34:37], v[86:89], v[206:221]
	v_fma_f32 v22, v173, |v2|, v22
	v_fma_f32 v23, v181, |v10|, v23
	v_fmac_f32_e32 v22, v175, v3
	v_fmac_f32_e32 v23, v183, v11
	v_fma_f32 v22, v175, |v3|, v22
	v_fma_f32 v23, v183, |v11|, v23
	v_fmac_f32_e32 v22, v170, v4
	v_fmac_f32_e32 v23, v178, v12
	v_fma_f32 v22, v170, |v4|, v22
	v_fma_f32 v23, v178, |v12|, v23
	v_mfma_f32_32x32x16_bf16 v[206:221], v[38:41], v[82:85], v[206:221]
	v_fmac_f32_e32 v22, v172, v5
	v_fmac_f32_e32 v23, v180, v13
	v_fma_f32 v22, v172, |v5|, v22
	v_fma_f32 v23, v180, |v13|, v23
	v_fmac_f32_e32 v22, v174, v6
	v_fmac_f32_e32 v23, v182, v14
	v_fma_f32 v22, v174, |v6|, v22
	v_fma_f32 v23, v182, |v14|, v23
	v_fmac_f32_e32 v22, v176, v7
	v_fmac_f32_e32 v23, v184, v15
	v_mfma_f32_32x32x16_bf16 v[206:221], v[46:49], v[74:77], v[206:221]
	v_fma_f32 v22, v176, |v7|, v22
	v_fma_f32 v23, v184, |v15|, v23
	s_nop 1
	v_permlane32_swap_b32_e32 v22, v23
	v_add_f32_e32 v24, v22, v23
	v_cvt_f16_f32_e32 v24, v24
	v_ashrrev_i16_e32 v25, 15, v24
	v_bitop3_b32 v26, v24, v25, s64 bitop3:0x1e
	v_or_b32_sdwa v27, v149, v26 dst_sel:DWORD dst_unused:UNUSED_PAD src0_sel:DWORD src1_sel:BYTE_1
	v_cndmask_b32_e64 v27, v239, v27, s[46:47]
	ds_write_b16 v202, v26 offset:1024
	v_lshl_add_u32 v27, v27, 2, s63
	ds_add_u32 v27, v187
	s_add_i32 s11, s11, 1
.Lq_end:
	v_add_u32_e32 v203, 0x300, v203
	v_add_u32_e32 v202, 0x600, v202
	v_add_u32_e32 v237, 0x600, v237
	s_add_i32 s10, s10, 24
	s_cmp_lt_u32 s11, s9
	s_cbranch_scc1 .Lq_loop
	s_waitcnt vmcnt(0)
	s_setprio 0
	s_branch .LBB0_434
